# cfgL + non-temporal (streaming) hint on the final phase's f32 output stores
# speedup vs baseline: 1.0044x; 1.0044x over previous
.LBB0_2269:
	s_waitcnt vmcnt(4)
	v_pk_mul_f32 v[84:85], v[40:41], v[16:17] op_sel_hi:[0,1]
	s_waitcnt vmcnt(0)
	v_cvt_f32_f16_sdwa v17, v14 dst_sel:DWORD dst_unused:UNUSED_PAD src0_sel:WORD_1
	v_cvt_f32_f16_e32 v16, v14
	v_pk_mul_f32 v[78:79], v[40:41], v[78:79] op_sel_hi:[0,1]
	v_pk_mul_f32 v[34:35], v[40:41], v[68:69] op_sel_hi:[0,1]
	v_mov_b32_e32 v68, v41
	v_pk_fma_f32 v[16:17], v[16:17], s[10:11], v[78:79] op_sel_hi:[1,0,1]
	v_cvt_f32_f16_sdwa v79, v0 dst_sel:DWORD dst_unused:UNUSED_PAD src0_sel:WORD_1
	v_cvt_f32_f16_e32 v78, v0
	v_and_b32_e32 v14, 64, v175
	v_pk_fma_f32 v[16:17], v[68:69], v[82:83], v[16:17] op_sel_hi:[0,1,1]
	v_add_u32_e32 v69, 64, v14
	v_xor_b32_e32 v14, 32, v175
	v_cvt_f32_f16_sdwa v83, v1 dst_sel:DWORD dst_unused:UNUSED_PAD src0_sel:WORD_1
	v_cvt_f32_f16_e32 v82, v1
	v_cmp_lt_i32_e32 vcc, v14, v69
	v_pk_fma_f32 v[78:79], v[78:79], s[10:11], v[84:85] op_sel_hi:[1,0,1]
	v_pk_mul_f32 v[18:19], v[40:41], v[18:19] op_sel_hi:[0,1]
	v_cndmask_b32_e32 v0, v175, v14, vcc
	v_pk_fma_f32 v[28:29], v[68:69], v[28:29], v[78:79] op_sel_hi:[0,1,1]
	v_lshlrev_b32_e32 v86, 2, v0
	v_add_f32_e32 v0, 0, v28
	v_add_f32_e32 v14, v29, v0
	v_pk_fma_f32 v[0:1], v[82:83], s[10:11], v[18:19] op_sel_hi:[1,0,1]
	v_pk_mul_f32 v[74:75], v[40:41], v[74:75] op_sel_hi:[0,1]
	v_pk_fma_f32 v[18:19], v[68:69], v[30:31], v[0:1] op_sel_hi:[0,1,1]
	v_cvt_f32_f16_sdwa v1, v15 dst_sel:DWORD dst_unused:UNUSED_PAD src0_sel:WORD_1
	v_cvt_f32_f16_e32 v0, v15
	v_add_f32_e32 v30, v18, v14
	v_cvt_f32_f16_sdwa v15, v2 dst_sel:DWORD dst_unused:UNUSED_PAD src0_sel:WORD_1
	v_cvt_f32_f16_e32 v14, v2
	v_pk_mul_f32 v[20:21], v[40:41], v[20:21] op_sel_hi:[0,1]
	v_pk_fma_f32 v[0:1], v[0:1], s[10:11], v[74:75] op_sel_hi:[1,0,1]
	v_add_f32_e32 v2, v19, v30
	v_pk_fma_f32 v[30:31], v[68:69], v[80:81], v[0:1] op_sel_hi:[0,1,1]
	v_pk_fma_f32 v[0:1], v[14:15], s[10:11], v[20:21] op_sel_hi:[1,0,1]
	v_cvt_f32_f16_sdwa v15, v3 dst_sel:DWORD dst_unused:UNUSED_PAD src0_sel:WORD_1
	v_cvt_f32_f16_e32 v14, v3
	v_pk_fma_f32 v[20:21], v[68:69], v[26:27], v[0:1] op_sel_hi:[0,1,1]
	v_pk_mul_f32 v[22:23], v[40:41], v[22:23] op_sel_hi:[0,1]
	v_add_f32_e32 v0, v20, v2
	v_cvt_f32_f16_sdwa v3, v4 dst_sel:DWORD dst_unused:UNUSED_PAD src0_sel:WORD_1
	v_cvt_f32_f16_e32 v2, v4
	v_add_f32_e32 v26, v21, v0
	v_pk_fma_f32 v[0:1], v[14:15], s[10:11], v[22:23] op_sel_hi:[1,0,1]
	v_pk_mul_f32 v[36:37], v[40:41], v[36:37] op_sel_hi:[0,1]
	v_pk_fma_f32 v[14:15], v[68:69], v[24:25], v[0:1] op_sel_hi:[0,1,1]
	v_add_f32_e32 v0, v14, v26
	v_add_f32_e32 v4, v15, v0
	v_pk_fma_f32 v[0:1], v[2:3], s[10:11], v[36:37] op_sel_hi:[1,0,1]
	v_cvt_f32_f16_sdwa v3, v5 dst_sel:DWORD dst_unused:UNUSED_PAD src0_sel:WORD_1
	v_cvt_f32_f16_e32 v2, v5
	v_pk_fma_f32 v[22:23], v[68:69], v[52:53], v[0:1] op_sel_hi:[0,1,1]
	v_pk_mul_f32 v[38:39], v[40:41], v[38:39] op_sel_hi:[0,1]
	v_add_f32_e32 v0, v4, v22
	v_add_f32_e32 v4, v23, v0
	v_pk_fma_f32 v[0:1], v[2:3], s[10:11], v[38:39] op_sel_hi:[1,0,1]
	v_cvt_f32_f16_sdwa v3, v6 dst_sel:DWORD dst_unused:UNUSED_PAD src0_sel:WORD_1
	v_cvt_f32_f16_e32 v2, v6
	v_pk_fma_f32 v[24:25], v[68:69], v[50:51], v[0:1] op_sel_hi:[0,1,1]
	v_pk_mul_f32 v[44:45], v[40:41], v[44:45] op_sel_hi:[0,1]
	v_add_f32_e32 v0, v24, v4
	v_add_f32_e32 v4, v25, v0
	v_pk_fma_f32 v[0:1], v[2:3], s[10:11], v[44:45] op_sel_hi:[1,0,1]
	v_cvt_f32_f16_sdwa v3, v7 dst_sel:DWORD dst_unused:UNUSED_PAD src0_sel:WORD_1
	v_cvt_f32_f16_e32 v2, v7
	v_pk_fma_f32 v[26:27], v[68:69], v[46:47], v[0:1] op_sel_hi:[0,1,1]
	v_pk_mul_f32 v[48:49], v[40:41], v[48:49] op_sel_hi:[0,1]
	v_add_f32_e32 v0, v26, v4
	v_add_f32_e32 v4, v27, v0
	v_pk_fma_f32 v[0:1], v[2:3], s[10:11], v[48:49] op_sel_hi:[1,0,1]
	v_cvt_f32_f16_sdwa v3, v8 dst_sel:DWORD dst_unused:UNUSED_PAD src0_sel:WORD_1
	v_cvt_f32_f16_e32 v2, v8
	v_pk_fma_f32 v[36:37], v[68:69], v[42:43], v[0:1] op_sel_hi:[0,1,1]
	v_pk_mul_f32 v[62:63], v[40:41], v[62:63] op_sel_hi:[0,1]
	v_add_f32_e32 v0, v36, v4
	v_add_f32_e32 v4, v37, v0
	v_pk_fma_f32 v[0:1], v[2:3], s[10:11], v[62:63] op_sel_hi:[1,0,1]
	v_cvt_f32_f16_sdwa v3, v9 dst_sel:DWORD dst_unused:UNUSED_PAD src0_sel:WORD_1
	v_cvt_f32_f16_e32 v2, v9
	v_pk_fma_f32 v[8:9], v[68:69], v[60:61], v[0:1] op_sel_hi:[0,1,1]
	v_pk_mul_f32 v[64:65], v[40:41], v[64:65] op_sel_hi:[0,1]
	v_add_f32_e32 v0, v4, v8
	v_add_f32_e32 v4, v9, v0
	v_pk_fma_f32 v[0:1], v[2:3], s[10:11], v[64:65] op_sel_hi:[1,0,1]
	v_cvt_f32_f16_sdwa v3, v10 dst_sel:DWORD dst_unused:UNUSED_PAD src0_sel:WORD_1
	v_cvt_f32_f16_e32 v2, v10
	v_pk_fma_f32 v[38:39], v[68:69], v[58:59], v[0:1] op_sel_hi:[0,1,1]
	v_pk_mul_f32 v[66:67], v[40:41], v[66:67] op_sel_hi:[0,1]
	v_add_f32_e32 v0, v38, v4
	v_add_f32_e32 v4, v39, v0
	v_pk_fma_f32 v[0:1], v[2:3], s[10:11], v[66:67] op_sel_hi:[1,0,1]
	v_cvt_f32_f16_sdwa v3, v11 dst_sel:DWORD dst_unused:UNUSED_PAD src0_sel:WORD_1
	v_cvt_f32_f16_e32 v2, v11
	v_pk_fma_f32 v[10:11], v[68:69], v[56:57], v[0:1] op_sel_hi:[0,1,1]
	v_add_f32_e32 v0, v10, v4
	v_add_f32_e32 v4, v11, v0
	v_pk_fma_f32 v[0:1], v[2:3], s[10:11], v[34:35] op_sel_hi:[1,0,1]
	v_cvt_f32_f16_sdwa v3, v12 dst_sel:DWORD dst_unused:UNUSED_PAD src0_sel:WORD_1
	v_cvt_f32_f16_e32 v2, v12
	v_pk_fma_f32 v[34:35], v[68:69], v[54:55], v[0:1] op_sel_hi:[0,1,1]
	v_pk_mul_f32 v[72:73], v[40:41], v[72:73] op_sel_hi:[0,1]
	v_add_f32_e32 v0, v34, v4
	v_add_f32_e32 v4, v35, v0
	v_pk_fma_f32 v[0:1], v[2:3], s[10:11], v[72:73] op_sel_hi:[1,0,1]
	v_cvt_f32_f16_sdwa v3, v13 dst_sel:DWORD dst_unused:UNUSED_PAD src0_sel:WORD_1
	v_cvt_f32_f16_e32 v2, v13
	v_pk_fma_f32 v[12:13], v[68:69], v[70:71], v[0:1] op_sel_hi:[0,1,1]
	v_pk_mul_f32 v[76:77], v[40:41], v[76:77] op_sel_hi:[0,1]
	v_add_f32_e32 v0, v4, v12
	v_add_f32_e32 v4, v13, v0
	v_pk_fma_f32 v[0:1], v[2:3], s[10:11], v[76:77] op_sel_hi:[1,0,1]
	v_xor_b32_e32 v2, 16, v175
	v_pk_fma_f32 v[32:33], v[68:69], v[32:33], v[0:1] op_sel_hi:[0,1,1]
	v_add_f32_e32 v0, v32, v4
	v_add_f32_e32 v0, v33, v0
	v_add_f32_e32 v0, v16, v0
	v_add_f32_e32 v0, v17, v0
	v_add_f32_e32 v0, v30, v0
	v_add_f32_e32 v0, v31, v0
	ds_bpermute_b32 v1, v86, v0
	v_cmp_lt_i32_e32 vcc, v2, v69
	s_mov_b64 s[28:29], 0
	s_mov_b64 s[2:3], 0
	v_cndmask_b32_e32 v2, v175, v2, vcc
	v_lshlrev_b32_e32 v87, 2, v2
	s_waitcnt lgkmcnt(0)
	v_add_f32_e32 v0, v0, v1
	ds_bpermute_b32 v1, v87, v0
	v_xor_b32_e32 v2, 8, v175
	v_cmp_lt_i32_e32 vcc, v2, v69
	s_waitcnt lgkmcnt(0)
	v_add_f32_e32 v0, v0, v1
	v_cndmask_b32_e32 v2, v175, v2, vcc
	v_lshlrev_b32_e32 v88, 2, v2
	ds_bpermute_b32 v1, v88, v0
	v_xor_b32_e32 v2, 4, v175
	v_cmp_lt_i32_e32 vcc, v2, v69
	s_waitcnt lgkmcnt(0)
	v_add_f32_e32 v0, v0, v1
	v_cndmask_b32_e32 v2, v175, v2, vcc
	v_lshlrev_b32_e32 v89, 2, v2
	ds_bpermute_b32 v1, v89, v0
	v_xor_b32_e32 v2, 2, v175
	v_cmp_lt_i32_e32 vcc, v2, v69
	s_waitcnt lgkmcnt(0)
	v_add_f32_e32 v0, v0, v1
	v_cndmask_b32_e32 v2, v175, v2, vcc
	v_lshlrev_b32_e32 v90, 2, v2
	ds_bpermute_b32 v1, v90, v0
	v_xor_b32_e32 v2, 1, v175
	v_cmp_lt_i32_e32 vcc, v2, v69
	s_waitcnt lgkmcnt(0)
	v_add_f32_e32 v42, v0, v1
	v_cndmask_b32_e32 v2, v175, v2, vcc
	v_lshlrev_b32_e32 v91, 2, v2
	ds_bpermute_b32 v43, v91, v42
	global_load_dwordx4 v[0:3], v[122:123], off
	global_load_dwordx4 v[4:7], v[124:125], off
	s_waitcnt lgkmcnt(0)
	v_add_f32_e32 v42, v42, v43
	v_mul_f32_e32 v42, 0x3a000000, v42
	v_pk_add_f32 v[66:67], v[28:29], v[42:43] op_sel_hi:[1,0] neg_lo:[0,1] neg_hi:[0,1]
	v_pk_add_f32 v[68:69], v[18:19], v[42:43] op_sel_hi:[1,0] neg_lo:[0,1] neg_hi:[0,1]
	v_pk_mul_f32 v[28:29], v[66:67], v[66:67]
	v_pk_mul_f32 v[18:19], v[68:69], v[68:69]
	v_add_f32_e32 v28, v28, v29
	v_pk_add_f32 v[70:71], v[20:21], v[42:43] op_sel_hi:[1,0] neg_lo:[0,1] neg_hi:[0,1]
	v_add_f32_e32 v18, v18, v28
	v_pk_mul_f32 v[20:21], v[70:71], v[70:71]
	v_add_f32_e32 v18, v19, v18
	v_pk_add_f32 v[72:73], v[14:15], v[42:43] op_sel_hi:[1,0] neg_lo:[0,1] neg_hi:[0,1]
	v_add_f32_e32 v18, v20, v18
	v_pk_mul_f32 v[14:15], v[72:73], v[72:73]
	v_add_f32_e32 v18, v21, v18
	v_pk_add_f32 v[74:75], v[22:23], v[42:43] op_sel_hi:[1,0] neg_lo:[0,1] neg_hi:[0,1]
	v_add_f32_e32 v14, v14, v18
	v_pk_mul_f32 v[22:23], v[74:75], v[74:75]
	v_add_f32_e32 v14, v15, v14
	v_pk_add_f32 v[76:77], v[24:25], v[42:43] op_sel_hi:[1,0] neg_lo:[0,1] neg_hi:[0,1]
	v_add_f32_e32 v14, v22, v14
	v_pk_mul_f32 v[24:25], v[76:77], v[76:77]
	v_add_f32_e32 v14, v23, v14
	v_pk_add_f32 v[78:79], v[26:27], v[42:43] op_sel_hi:[1,0] neg_lo:[0,1] neg_hi:[0,1]
	v_add_f32_e32 v14, v24, v14
	v_pk_mul_f32 v[26:27], v[78:79], v[78:79]
	v_add_f32_e32 v14, v25, v14
	v_pk_add_f32 v[80:81], v[36:37], v[42:43] op_sel_hi:[1,0] neg_lo:[0,1] neg_hi:[0,1]
	v_add_f32_e32 v14, v26, v14
	v_pk_mul_f32 v[36:37], v[80:81], v[80:81]
	v_add_f32_e32 v14, v27, v14
	v_pk_add_f32 v[82:83], v[8:9], v[42:43] op_sel_hi:[1,0] neg_lo:[0,1] neg_hi:[0,1]
	v_add_f32_e32 v14, v36, v14
	v_pk_mul_f32 v[8:9], v[82:83], v[82:83]
	v_add_f32_e32 v14, v37, v14
	v_pk_add_f32 v[84:85], v[38:39], v[42:43] op_sel_hi:[1,0] neg_lo:[0,1] neg_hi:[0,1]
	v_add_f32_e32 v8, v8, v14
	v_pk_mul_f32 v[38:39], v[84:85], v[84:85]
	v_add_f32_e32 v8, v9, v8
	v_pk_add_f32 v[92:93], v[10:11], v[42:43] op_sel_hi:[1,0] neg_lo:[0,1] neg_hi:[0,1]
	v_add_f32_e32 v8, v38, v8
	v_pk_mul_f32 v[10:11], v[92:93], v[92:93]
	v_add_f32_e32 v8, v39, v8
	v_pk_add_f32 v[94:95], v[34:35], v[42:43] op_sel_hi:[1,0] neg_lo:[0,1] neg_hi:[0,1]
	v_add_f32_e32 v8, v10, v8
	v_pk_mul_f32 v[34:35], v[94:95], v[94:95]
	v_add_f32_e32 v8, v11, v8
	v_pk_add_f32 v[96:97], v[12:13], v[42:43] op_sel_hi:[1,0] neg_lo:[0,1] neg_hi:[0,1]
	v_add_f32_e32 v8, v34, v8
	v_pk_mul_f32 v[12:13], v[96:97], v[96:97]
	v_add_f32_e32 v8, v35, v8
	v_pk_add_f32 v[98:99], v[32:33], v[42:43] op_sel_hi:[1,0] neg_lo:[0,1] neg_hi:[0,1]
	v_add_f32_e32 v8, v12, v8
	v_pk_mul_f32 v[32:33], v[98:99], v[98:99]
	v_add_f32_e32 v8, v13, v8
	v_pk_add_f32 v[102:103], v[16:17], v[42:43] op_sel_hi:[1,0] neg_lo:[0,1] neg_hi:[0,1]
	v_add_f32_e32 v8, v32, v8
	v_pk_mul_f32 v[16:17], v[102:103], v[102:103]
	v_add_f32_e32 v8, v33, v8
	v_pk_add_f32 v[100:101], v[30:31], v[42:43] op_sel_hi:[1,0] neg_lo:[0,1] neg_hi:[0,1]
	v_add_f32_e32 v8, v16, v8
	v_pk_mul_f32 v[30:31], v[100:101], v[100:101]
	v_add_f32_e32 v8, v17, v8
	v_add_f32_e32 v8, v30, v8
	v_add_f32_e32 v20, v31, v8
	ds_bpermute_b32 v21, v86, v20
	global_load_dwordx4 v[8:11], v[122:123], off offset:16
	global_load_dwordx4 v[12:15], v[124:125], off offset:16
	global_load_dwordx4 v[16:19], v[124:125], off offset:2048
	s_waitcnt lgkmcnt(0)
	v_add_f32_e32 v32, v20, v21
	ds_bpermute_b32 v33, v87, v32
	global_load_dwordx4 v[20:23], v[122:123], off offset:2048
	global_load_dwordx4 v[24:27], v[122:123], off offset:2064
	global_load_dwordx4 v[28:31], v[124:125], off offset:2064
	s_waitcnt lgkmcnt(0)
	v_add_f32_e32 v42, v32, v33
	ds_bpermute_b32 v43, v88, v42
	global_load_dwordx4 v[32:35], v[126:127], off
	global_load_dwordx4 v[36:39], v[128:129], off
	s_waitcnt lgkmcnt(0)
	v_add_f32_e32 v42, v42, v43
	ds_bpermute_b32 v43, v89, v42
	s_waitcnt lgkmcnt(0)
	v_add_f32_e32 v54, v42, v43
	ds_bpermute_b32 v55, v90, v54
	global_load_dwordx4 v[42:45], v[126:127], off offset:16
	global_load_dwordx4 v[46:49], v[128:129], off offset:16
	global_load_dwordx4 v[50:53], v[132:133], off
	s_waitcnt lgkmcnt(0)
	v_add_f32_e32 v104, v54, v55
	global_load_dwordx4 v[54:57], v[130:131], off
	global_load_dwordx4 v[58:61], v[130:131], off offset:16
	global_load_dwordx4 v[62:65], v[132:133], off offset:16
	ds_bpermute_b32 v105, v91, v104
	s_waitcnt lgkmcnt(0)
	v_add_f32_e32 v104, v104, v105
	v_fmamk_f32 v104, v104, 0x3a000000, v173
	v_mul_f32_e32 v105, 0x4f800000, v104
	v_cmp_gt_f32_e32 vcc, s48, v104
	s_nop 1
	v_cndmask_b32_e32 v104, v104, v105, vcc
	v_sqrt_f32_e32 v105, v104
	s_nop 0
	v_add_u32_e32 v106, -1, v105
	v_fma_f32 v107, -v106, v105, v104
	v_cmp_ge_f32_e64 s[0:1], 0, v107
	v_add_u32_e32 v107, 1, v105
	s_nop 0
	v_cndmask_b32_e64 v106, v105, v106, s[0:1]
	v_fma_f32 v105, -v107, v105, v104
	v_cmp_lt_f32_e64 s[0:1], 0, v105
	s_nop 1
	v_cndmask_b32_e64 v105, v106, v107, s[0:1]
	v_mul_f32_e32 v106, 0x37800000, v105
	v_cndmask_b32_e32 v105, v105, v106, vcc
	v_cmp_class_f32_e32 vcc, v104, v174
	s_nop 1
	v_cndmask_b32_e32 v104, v105, v104, vcc
	v_div_scale_f32 v105, s[0:1], v104, v104, 1.0
	v_rcp_f32_e32 v106, v105
	s_lshl_b64 s[0:1], s[4:5], 13
	s_cmp_eq_u32 s12, s4
	v_fma_f32 v107, -v105, v106, 1.0
	v_fmac_f32_e32 v106, v107, v106
	v_div_scale_f32 v107, vcc, 1.0, v104, 1.0
	v_mul_f32_e32 v108, v107, v106
	v_fma_f32 v109, -v105, v108, v107
	v_fmac_f32_e32 v108, v109, v106
	v_fma_f32 v105, -v105, v108, v107
	v_div_fmas_f32 v105, v105, v106, v108
	v_div_fixup_f32 v104, v105, v104, 1.0
	v_pk_mul_f32 v[66:67], v[66:67], v[104:105] op_sel_hi:[1,0]
	v_pk_mul_f32 v[68:69], v[68:69], v[104:105] op_sel_hi:[1,0]
	s_waitcnt vmcnt(14)
	v_pk_fma_f32 v[0:1], v[0:1], v[66:67], v[4:5]
	v_pk_fma_f32 v[2:3], v[2:3], v[68:69], v[6:7]
	v_lshl_add_u64 v[4:5], v[118:119], 0, s[0:1]
	global_store_dwordx4 v[4:5], v[0:3], off nt
	s_nop 1
	v_pk_mul_f32 v[0:1], v[70:71], v[104:105] op_sel_hi:[1,0]
	v_pk_mul_f32 v[2:3], v[72:73], v[104:105] op_sel_hi:[1,0]
	s_waitcnt vmcnt(13)
	v_pk_fma_f32 v[0:1], v[8:9], v[0:1], v[12:13]
	v_pk_fma_f32 v[2:3], v[10:11], v[2:3], v[14:15]
	global_store_dwordx4 v[4:5], v[0:3], off offset:16 nt
	s_nop 1
	v_pk_mul_f32 v[0:1], v[74:75], v[104:105] op_sel_hi:[1,0]
	v_pk_mul_f32 v[2:3], v[76:77], v[104:105] op_sel_hi:[1,0]
	s_waitcnt vmcnt(12)
	v_pk_fma_f32 v[0:1], v[20:21], v[0:1], v[16:17]
	v_pk_fma_f32 v[2:3], v[22:23], v[2:3], v[18:19]
	global_store_dwordx4 v[4:5], v[0:3], off offset:2048 nt
	s_nop 1
	v_pk_mul_f32 v[0:1], v[78:79], v[104:105] op_sel_hi:[1,0]
	v_pk_mul_f32 v[2:3], v[80:81], v[104:105] op_sel_hi:[1,0]
	s_waitcnt vmcnt(11)
	v_pk_fma_f32 v[0:1], v[24:25], v[0:1], v[28:29]
	v_pk_fma_f32 v[2:3], v[26:27], v[2:3], v[30:31]
	global_store_dwordx4 v[4:5], v[0:3], off offset:2064 nt
	v_add_co_u32_e32 v4, vcc, s49, v4
	s_nop 0
	v_pk_mul_f32 v[0:1], v[82:83], v[104:105] op_sel_hi:[1,0]
	v_pk_mul_f32 v[2:3], v[84:85], v[104:105] op_sel_hi:[1,0]
	s_waitcnt vmcnt(10)
	v_pk_fma_f32 v[0:1], v[32:33], v[0:1], v[36:37]
	v_pk_fma_f32 v[2:3], v[34:35], v[2:3], v[38:39]
	v_addc_co_u32_e32 v5, vcc, 0, v5, vcc
	global_store_dwordx4 v[4:5], v[0:3], off nt
	s_nop 1
	v_pk_mul_f32 v[0:1], v[92:93], v[104:105] op_sel_hi:[1,0]
	v_pk_mul_f32 v[2:3], v[94:95], v[104:105] op_sel_hi:[1,0]
	s_waitcnt vmcnt(9)
	v_pk_fma_f32 v[0:1], v[42:43], v[0:1], v[46:47]
	v_pk_fma_f32 v[2:3], v[44:45], v[2:3], v[48:49]
	global_store_dwordx4 v[4:5], v[0:3], off offset:16 nt
	s_nop 1
	v_pk_mul_f32 v[0:1], v[96:97], v[104:105] op_sel_hi:[1,0]
	v_pk_mul_f32 v[2:3], v[98:99], v[104:105] op_sel_hi:[1,0]
	s_waitcnt vmcnt(8)
	v_pk_fma_f32 v[0:1], v[54:55], v[0:1], v[50:51]
	v_pk_fma_f32 v[2:3], v[56:57], v[2:3], v[52:53]
	global_store_dwordx4 v[4:5], v[0:3], off offset:2048 nt
	s_nop 1
	v_pk_mul_f32 v[0:1], v[102:103], v[104:105] op_sel_hi:[1,0]
	v_pk_mul_f32 v[2:3], v[100:101], v[104:105] op_sel_hi:[1,0]
	s_waitcnt vmcnt(7)
	v_pk_fma_f32 v[0:1], v[58:59], v[0:1], v[62:63]
	v_pk_fma_f32 v[2:3], v[60:61], v[2:3], v[64:65]
	global_store_dwordx4 v[4:5], v[0:3], off offset:2064 nt
	s_cbranch_scc1 .LBB0_2319
	s_lshl_b64 s[0:1], s[12:13], 12
	v_lshl_add_u64 v[12:13], v[134:135], 0, s[0:1]
	global_load_dwordx4 v[0:3], v[12:13], off
	s_sub_i32 s0, s15, s44
	s_lshl_b32 s19, s0, 3
	s_lshl_b32 s0, s50, 10
	s_ashr_i32 s15, s14, 31
	s_and_b32 s8, s0, 0x3fc00
	s_lshl_b64 s[0:1], s[14:15], 12
	s_add_u32 s30, s6, s0
	v_lshl_add_u64 v[32:33], v[120:121], 0, s[8:9]
	s_addc_u32 s31, s7, s1
	s_mov_b64 s[0:1], -1
	s_and_b64 vcc, exec, s[26:27]
	s_cbranch_vccz .LBB0_2274
	v_mov_b32_e32 v16, 0
	v_or_b32_e32 v4, s19, v115
	s_mov_b32 s0, s42
	v_mov_b32_e32 v17, v16
	v_mov_b32_e32 v18, v16
	v_mov_b32_e32 v19, v16
	v_mov_b32_e32 v20, v16
	v_mov_b32_e32 v21, v16
	v_mov_b32_e32 v22, v16
	v_mov_b32_e32 v23, v16

.LBB0_2319:
	s_and_b64 vcc, exec, s[28:29]
	s_cbranch_vccz .LBB0_2322
	s_waitcnt lgkmcnt(0)
	global_load_dwordx4 v[4:7], v116, s[22:23] offset:3072
	global_load_dwordx4 v[46:49], v116, s[22:23]
	s_ashr_i32 s21, s20, 31
	s_lshl_b64 s[0:1], s[20:21], 12
	s_ashr_i32 s19, s18, 31
	v_lshl_add_u64 v[0:1], v[136:137], 0, s[0:1]
	global_load_dwordx4 v[28:31], v116, s[22:23] offset:1024
	global_load_dwordx4 v[12:15], v[0:1], off offset:3072
	s_lshl_b64 s[18:19], s[18:19], 12
	v_lshl_add_u64 v[2:3], v[136:137], 0, s[18:19]
	global_load_dwordx4 v[8:11], v[2:3], off offset:3072
	global_load_dwordx4 v[50:53], v[0:1], off
	global_load_dwordx4 v[54:57], v[2:3], off
	global_load_dwordx4 v[36:39], v[0:1], off offset:1024
	global_load_dwordx4 v[24:27], v116, s[22:23] offset:2048
	global_load_dwordx4 v[20:23], v[0:1], off offset:2048
	global_load_dwordx4 v[16:19], v[2:3], off offset:2048
	global_load_dwordx4 v[32:35], v[2:3], off offset:1024
	v_and_b32_e32 v0, 64, v175
	v_xor_b32_e32 v45, 32, v175
	v_add_u32_e32 v80, 64, v0
	v_cmp_lt_i32_e32 vcc, v45, v80
	s_waitcnt vmcnt(12)
	v_mov_b32_e32 v44, v41
	s_ashr_i32 s15, s14, 31
	v_cndmask_b32_e32 v45, v175, v45, vcc
	v_lshlrev_b32_e32 v176, 2, v45
	s_lshl_b64 s[14:15], s[14:15], 12
	s_lshl_b64 s[18:19], s[12:13], 12
	s_ashr_i32 s17, s16, 31
	s_lshl_b64 s[0:1], s[16:17], 12
	v_lshl_add_u64 v[42:43], v[134:135], 0, s[18:19]
	global_load_dwordx4 v[0:3], v[42:43], off
	global_load_dwordx4 v[104:107], v[42:43], off offset:1024
	s_waitcnt vmcnt(13)
	v_cvt_f32_f16_e32 v58, v6
	s_waitcnt vmcnt(12)
	v_cvt_f32_f16_e32 v60, v46
	v_cvt_f32_f16_sdwa v61, v46 dst_sel:DWORD dst_unused:UNUSED_PAD src0_sel:WORD_1
	v_cvt_f32_f16_e32 v46, v47
	s_waitcnt vmcnt(8)
	v_cvt_f32_f16_e32 v70, v50
	v_cvt_f32_f16_sdwa v71, v50 dst_sel:DWORD dst_unused:UNUSED_PAD src0_sel:WORD_1
	v_cvt_f32_f16_e32 v50, v51
	v_cvt_f32_f16_sdwa v51, v51 dst_sel:DWORD dst_unused:UNUSED_PAD src0_sel:WORD_1
	v_cvt_f32_f16_sdwa v47, v47 dst_sel:DWORD dst_unused:UNUSED_PAD src0_sel:WORD_1
	s_waitcnt vmcnt(7)
	v_cvt_f32_f16_e32 v72, v54
	v_cvt_f32_f16_sdwa v73, v54 dst_sel:DWORD dst_unused:UNUSED_PAD src0_sel:WORD_1
	v_cvt_f32_f16_e32 v66, v14
	v_cvt_f32_f16_sdwa v67, v14 dst_sel:DWORD dst_unused:UNUSED_PAD src0_sel:WORD_1
	v_cvt_f32_f16_e32 v54, v55
	v_cvt_f32_f16_sdwa v55, v55 dst_sel:DWORD dst_unused:UNUSED_PAD src0_sel:WORD_1
	v_cvt_f32_f16_e32 v14, v15
	v_cvt_f32_f16_sdwa v15, v15 dst_sel:DWORD dst_unused:UNUSED_PAD src0_sel:WORD_1
	v_cvt_f32_f16_e32 v74, v52
	v_cvt_f32_f16_sdwa v75, v52 dst_sel:DWORD dst_unused:UNUSED_PAD src0_sel:WORD_1
	v_cvt_f32_f16_e32 v52, v53
	v_cvt_f32_f16_sdwa v53, v53 dst_sel:DWORD dst_unused:UNUSED_PAD src0_sel:WORD_1
	v_pk_mul_f32 v[70:71], v[40:41], v[70:71] op_sel_hi:[0,1]
	v_cvt_f32_f16_sdwa v59, v6 dst_sel:DWORD dst_unused:UNUSED_PAD src0_sel:WORD_1
	v_cvt_f32_f16_e32 v6, v7
	v_cvt_f32_f16_sdwa v7, v7 dst_sel:DWORD dst_unused:UNUSED_PAD src0_sel:WORD_1
	v_cvt_f32_f16_e32 v62, v48
	v_cvt_f32_f16_sdwa v63, v48 dst_sel:DWORD dst_unused:UNUSED_PAD src0_sel:WORD_1
	v_cvt_f32_f16_e32 v48, v49
	v_cvt_f32_f16_sdwa v49, v49 dst_sel:DWORD dst_unused:UNUSED_PAD src0_sel:WORD_1
	v_pk_mul_f32 v[50:51], v[40:41], v[50:51] op_sel_hi:[0,1]
	v_pk_fma_f32 v[60:61], v[60:61], s[10:11], v[70:71] op_sel_hi:[1,0,1]
	v_cvt_f32_f16_e32 v68, v10
	v_cvt_f32_f16_sdwa v69, v10 dst_sel:DWORD dst_unused:UNUSED_PAD src0_sel:WORD_1
	v_cvt_f32_f16_e32 v10, v11
	v_cvt_f32_f16_sdwa v11, v11 dst_sel:DWORD dst_unused:UNUSED_PAD src0_sel:WORD_1
	v_cvt_f32_f16_e32 v76, v56
	v_cvt_f32_f16_sdwa v77, v56 dst_sel:DWORD dst_unused:UNUSED_PAD src0_sel:WORD_1
	v_cvt_f32_f16_e32 v56, v57
	v_cvt_f32_f16_sdwa v57, v57 dst_sel:DWORD dst_unused:UNUSED_PAD src0_sel:WORD_1
	v_pk_fma_f32 v[46:47], v[46:47], s[10:11], v[50:51] op_sel_hi:[1,0,1]
	v_pk_fma_f32 v[50:51], v[44:45], v[72:73], v[60:61] op_sel_hi:[0,1,1]
	v_cvt_f32_f16_e32 v64, v28
	v_cvt_f32_f16_sdwa v65, v28 dst_sel:DWORD dst_unused:UNUSED_PAD src0_sel:WORD_1
	v_add_f32_e32 v28, 0, v50
	s_waitcnt vmcnt(6)
	v_cvt_f32_f16_e32 v78, v36
	v_cvt_f32_f16_sdwa v79, v36 dst_sel:DWORD dst_unused:UNUSED_PAD src0_sel:WORD_1
	v_pk_mul_f32 v[14:15], v[40:41], v[14:15] op_sel_hi:[0,1]
	v_pk_mul_f32 v[74:75], v[40:41], v[74:75] op_sel_hi:[0,1]
	v_pk_mul_f32 v[52:53], v[40:41], v[52:53] op_sel_hi:[0,1]
	v_pk_fma_f32 v[46:47], v[44:45], v[54:55], v[46:47] op_sel_hi:[0,1,1]
	v_add_f32_e32 v28, v51, v28
	v_pk_fma_f32 v[14:15], v[6:7], s[10:11], v[14:15] op_sel_hi:[1,0,1]
	v_pk_fma_f32 v[62:63], v[62:63], s[10:11], v[74:75] op_sel_hi:[1,0,1]
	v_pk_fma_f32 v[52:53], v[48:49], s[10:11], v[52:53] op_sel_hi:[1,0,1]
	v_add_f32_e32 v28, v46, v28
	v_pk_fma_f32 v[10:11], v[44:45], v[10:11], v[14:15] op_sel_hi:[0,1,1]
	v_pk_fma_f32 v[48:49], v[44:45], v[76:77], v[62:63] op_sel_hi:[0,1,1]
	v_pk_fma_f32 v[14:15], v[44:45], v[56:57], v[52:53] op_sel_hi:[0,1,1]
	v_add_f32_e32 v28, v47, v28
	s_waitcnt vmcnt(2)
	v_cvt_f32_f16_e32 v52, v32
	v_cvt_f32_f16_sdwa v53, v32 dst_sel:DWORD dst_unused:UNUSED_PAD src0_sel:WORD_1
	v_add_f32_e32 v28, v48, v28
	v_add_f32_e32 v28, v49, v28
	v_pk_mul_f32 v[54:55], v[40:41], v[78:79] op_sel_hi:[0,1]
	v_pk_mul_f32 v[66:67], v[40:41], v[66:67] op_sel_hi:[0,1]
	v_add_f32_e32 v28, v14, v28
	v_pk_fma_f32 v[54:55], v[64:65], s[10:11], v[54:55] op_sel_hi:[1,0,1]
	v_pk_fma_f32 v[58:59], v[58:59], s[10:11], v[66:67] op_sel_hi:[1,0,1]
	v_add_f32_e32 v28, v15, v28
	v_pk_fma_f32 v[52:53], v[44:45], v[52:53], v[54:55] op_sel_hi:[0,1,1]
	v_cvt_f32_f16_e32 v36, v37
	v_cvt_f32_f16_sdwa v37, v37 dst_sel:DWORD dst_unused:UNUSED_PAD src0_sel:WORD_1
	v_pk_fma_f32 v[6:7], v[44:45], v[68:69], v[58:59] op_sel_hi:[0,1,1]
	v_add_f32_e32 v45, v52, v28
	v_cvt_f32_f16_e32 v28, v29
	v_cvt_f32_f16_sdwa v29, v29 dst_sel:DWORD dst_unused:UNUSED_PAD src0_sel:WORD_1
	v_cvt_f32_f16_e32 v32, v33
	v_cvt_f32_f16_sdwa v33, v33 dst_sel:DWORD dst_unused:UNUSED_PAD src0_sel:WORD_1
	v_pk_mul_f32 v[36:37], v[40:41], v[36:37] op_sel_hi:[0,1]
	v_add_f32_e32 v45, v53, v45
	v_pk_fma_f32 v[28:29], v[28:29], s[10:11], v[36:37] op_sel_hi:[1,0,1]
	v_cvt_f32_f16_e32 v36, v38
	v_cvt_f32_f16_sdwa v37, v38 dst_sel:DWORD dst_unused:UNUSED_PAD src0_sel:WORD_1
	v_pk_fma_f32 v[28:29], v[44:45], v[32:33], v[28:29] op_sel_hi:[0,1,1]
	v_cvt_f32_f16_e32 v32, v30
	v_cvt_f32_f16_sdwa v33, v30 dst_sel:DWORD dst_unused:UNUSED_PAD src0_sel:WORD_1
	v_cvt_f32_f16_e32 v54, v34
	v_cvt_f32_f16_sdwa v55, v34 dst_sel:DWORD dst_unused:UNUSED_PAD src0_sel:WORD_1
	v_pk_mul_f32 v[36:37], v[40:41], v[36:37] op_sel_hi:[0,1]
	v_add_f32_e32 v45, v28, v45
	v_pk_fma_f32 v[32:33], v[32:33], s[10:11], v[36:37] op_sel_hi:[1,0,1]
	v_add_f32_e32 v30, v29, v45
	v_pk_fma_f32 v[32:33], v[44:45], v[54:55], v[32:33] op_sel_hi:[0,1,1]
	v_cvt_f32_f16_e32 v36, v39
	v_cvt_f32_f16_sdwa v37, v39 dst_sel:DWORD dst_unused:UNUSED_PAD src0_sel:WORD_1
	v_add_f32_e32 v38, v32, v30
	v_cvt_f32_f16_e32 v30, v31
	v_cvt_f32_f16_sdwa v31, v31 dst_sel:DWORD dst_unused:UNUSED_PAD src0_sel:WORD_1
	v_cvt_f32_f16_e32 v34, v35
	v_cvt_f32_f16_sdwa v35, v35 dst_sel:DWORD dst_unused:UNUSED_PAD src0_sel:WORD_1
	v_pk_mul_f32 v[36:37], v[40:41], v[36:37] op_sel_hi:[0,1]
	v_pk_fma_f32 v[30:31], v[30:31], s[10:11], v[36:37] op_sel_hi:[1,0,1]
	v_cvt_f32_f16_e32 v36, v20
	v_cvt_f32_f16_sdwa v37, v20 dst_sel:DWORD dst_unused:UNUSED_PAD src0_sel:WORD_1
	v_add_f32_e32 v38, v33, v38
	v_pk_fma_f32 v[30:31], v[44:45], v[34:35], v[30:31] op_sel_hi:[0,1,1]
	v_cvt_f32_f16_e32 v34, v24
	v_cvt_f32_f16_sdwa v35, v24 dst_sel:DWORD dst_unused:UNUSED_PAD src0_sel:WORD_1
	v_add_f32_e32 v45, v30, v38
	v_cvt_f32_f16_e32 v38, v16
	v_cvt_f32_f16_sdwa v39, v16 dst_sel:DWORD dst_unused:UNUSED_PAD src0_sel:WORD_1
	v_pk_mul_f32 v[36:37], v[40:41], v[36:37] op_sel_hi:[0,1]
	v_pk_fma_f32 v[34:35], v[34:35], s[10:11], v[36:37] op_sel_hi:[1,0,1]
	v_cvt_f32_f16_e32 v20, v21
	v_cvt_f32_f16_sdwa v21, v21 dst_sel:DWORD dst_unused:UNUSED_PAD src0_sel:WORD_1
	v_add_f32_e32 v16, v31, v45
	v_pk_fma_f32 v[34:35], v[44:45], v[38:39], v[34:35] op_sel_hi:[0,1,1]
	v_cvt_f32_f16_e32 v24, v25
	v_cvt_f32_f16_sdwa v25, v25 dst_sel:DWORD dst_unused:UNUSED_PAD src0_sel:WORD_1
	v_add_f32_e32 v36, v34, v16
	v_cvt_f32_f16_e32 v16, v17
	v_cvt_f32_f16_sdwa v17, v17 dst_sel:DWORD dst_unused:UNUSED_PAD src0_sel:WORD_1
	v_pk_mul_f32 v[20:21], v[40:41], v[20:21] op_sel_hi:[0,1]
	v_pk_fma_f32 v[20:21], v[24:25], s[10:11], v[20:21] op_sel_hi:[1,0,1]
	v_cvt_f32_f16_e32 v24, v22
	v_cvt_f32_f16_sdwa v25, v22 dst_sel:DWORD dst_unused:UNUSED_PAD src0_sel:WORD_1
	v_add_f32_e32 v36, v35, v36
	v_pk_fma_f32 v[16:17], v[44:45], v[16:17], v[20:21] op_sel_hi:[0,1,1]
	v_cvt_f32_f16_e32 v20, v26
	v_cvt_f32_f16_sdwa v21, v26 dst_sel:DWORD dst_unused:UNUSED_PAD src0_sel:WORD_1
	v_add_f32_e32 v38, v16, v36
	v_cvt_f32_f16_e32 v36, v18
	v_cvt_f32_f16_sdwa v37, v18 dst_sel:DWORD dst_unused:UNUSED_PAD src0_sel:WORD_1
	v_pk_mul_f32 v[24:25], v[40:41], v[24:25] op_sel_hi:[0,1]
	v_pk_fma_f32 v[20:21], v[20:21], s[10:11], v[24:25] op_sel_hi:[1,0,1]
	v_cvt_f32_f16_e32 v22, v23
	v_cvt_f32_f16_sdwa v23, v23 dst_sel:DWORD dst_unused:UNUSED_PAD src0_sel:WORD_1
	v_add_f32_e32 v18, v17, v38
	v_pk_fma_f32 v[20:21], v[44:45], v[36:37], v[20:21] op_sel_hi:[0,1,1]
	v_cvt_f32_f16_e32 v24, v27
	v_cvt_f32_f16_sdwa v25, v27 dst_sel:DWORD dst_unused:UNUSED_PAD src0_sel:WORD_1
	v_add_f32_e32 v26, v20, v18
	v_cvt_f32_f16_e32 v18, v19
	v_cvt_f32_f16_sdwa v19, v19 dst_sel:DWORD dst_unused:UNUSED_PAD src0_sel:WORD_1
	v_pk_mul_f32 v[22:23], v[40:41], v[22:23] op_sel_hi:[0,1]
	v_pk_fma_f32 v[22:23], v[24:25], s[10:11], v[22:23] op_sel_hi:[1,0,1]
	v_cvt_f32_f16_e32 v24, v12
	v_cvt_f32_f16_sdwa v25, v12 dst_sel:DWORD dst_unused:UNUSED_PAD src0_sel:WORD_1
	v_add_f32_e32 v26, v21, v26
	v_pk_fma_f32 v[18:19], v[44:45], v[18:19], v[22:23] op_sel_hi:[0,1,1]
	v_cvt_f32_f16_e32 v22, v4
	v_cvt_f32_f16_sdwa v23, v4 dst_sel:DWORD dst_unused:UNUSED_PAD src0_sel:WORD_1
	v_add_f32_e32 v36, v18, v26
	v_cvt_f32_f16_e32 v26, v8
	v_cvt_f32_f16_sdwa v27, v8 dst_sel:DWORD dst_unused:UNUSED_PAD src0_sel:WORD_1
	v_pk_mul_f32 v[24:25], v[40:41], v[24:25] op_sel_hi:[0,1]
	v_pk_fma_f32 v[22:23], v[22:23], s[10:11], v[24:25] op_sel_hi:[1,0,1]
	v_add_f32_e32 v4, v19, v36
	v_pk_fma_f32 v[22:23], v[44:45], v[26:27], v[22:23] op_sel_hi:[0,1,1]
	v_cvt_f32_f16_e32 v12, v13
	v_cvt_f32_f16_sdwa v13, v13 dst_sel:DWORD dst_unused:UNUSED_PAD src0_sel:WORD_1
	v_add_f32_e32 v24, v22, v4
	v_cvt_f32_f16_e32 v4, v5
	v_cvt_f32_f16_sdwa v5, v5 dst_sel:DWORD dst_unused:UNUSED_PAD src0_sel:WORD_1
	v_cvt_f32_f16_e32 v8, v9
	v_cvt_f32_f16_sdwa v9, v9 dst_sel:DWORD dst_unused:UNUSED_PAD src0_sel:WORD_1
	v_pk_mul_f32 v[12:13], v[40:41], v[12:13] op_sel_hi:[0,1]
	v_pk_fma_f32 v[4:5], v[4:5], s[10:11], v[12:13] op_sel_hi:[1,0,1]
	v_add_f32_e32 v24, v23, v24
	v_pk_fma_f32 v[4:5], v[44:45], v[8:9], v[4:5] op_sel_hi:[0,1,1]
	v_add_f32_e32 v8, v4, v24
	v_add_f32_e32 v8, v5, v8
	v_add_f32_e32 v8, v6, v8
	v_add_f32_e32 v8, v7, v8
	v_add_f32_e32 v8, v10, v8
	v_add_f32_e32 v8, v11, v8
	ds_bpermute_b32 v9, v176, v8
	v_xor_b32_e32 v12, 16, v175
	v_cmp_lt_i32_e32 vcc, v12, v80
	s_waitcnt lgkmcnt(0)
	v_add_f32_e32 v8, v8, v9
	v_cndmask_b32_e32 v12, v175, v12, vcc
	v_lshlrev_b32_e32 v177, 2, v12
	ds_bpermute_b32 v9, v177, v8
	v_xor_b32_e32 v12, 8, v175
	v_cmp_lt_i32_e32 vcc, v12, v80
	s_waitcnt lgkmcnt(0)
	v_add_f32_e32 v8, v8, v9
	v_cndmask_b32_e32 v12, v175, v12, vcc
	v_lshlrev_b32_e32 v178, 2, v12
	ds_bpermute_b32 v9, v178, v8
	v_xor_b32_e32 v12, 4, v175
	v_cmp_lt_i32_e32 vcc, v12, v80
	s_waitcnt lgkmcnt(0)
	v_add_f32_e32 v8, v8, v9
	v_cndmask_b32_e32 v12, v175, v12, vcc
	v_lshlrev_b32_e32 v179, 2, v12
	ds_bpermute_b32 v9, v179, v8
	v_xor_b32_e32 v12, 2, v175
	v_cmp_lt_i32_e32 vcc, v12, v80
	s_waitcnt lgkmcnt(0)
	v_add_f32_e32 v8, v8, v9
	v_cndmask_b32_e32 v12, v175, v12, vcc
	v_lshlrev_b32_e32 v180, 2, v12
	ds_bpermute_b32 v9, v180, v8
	v_xor_b32_e32 v12, 1, v175
	v_cmp_lt_i32_e32 vcc, v12, v80
	s_waitcnt lgkmcnt(0)
	v_add_f32_e32 v24, v8, v9
	v_cndmask_b32_e32 v12, v175, v12, vcc
	v_lshlrev_b32_e32 v181, 2, v12
	ds_bpermute_b32 v25, v181, v24
	v_lshl_add_u64 v[8:9], v[136:137], 0, s[14:15]
	global_load_dwordx4 v[108:111], v[8:9], off
	v_lshl_add_u64 v[12:13], v[136:137], 0, s[0:1]
	global_load_dwordx4 v[100:103], v[12:13], off
	s_waitcnt lgkmcnt(0)
	v_add_f32_e32 v24, v24, v25
	v_mul_f32_e32 v24, 0x3a000000, v24
	v_pk_add_f32 v[166:167], v[50:51], v[24:25] op_sel_hi:[1,0] neg_lo:[0,1] neg_hi:[0,1]
	v_pk_add_f32 v[168:169], v[46:47], v[24:25] op_sel_hi:[1,0] neg_lo:[0,1] neg_hi:[0,1]
	v_pk_mul_f32 v[26:27], v[166:167], v[166:167]
	v_pk_mul_f32 v[36:37], v[168:169], v[168:169]
	v_pk_add_f32 v[162:163], v[48:49], v[24:25] op_sel_hi:[1,0] neg_lo:[0,1] neg_hi:[0,1]
	v_pk_add_f32 v[164:165], v[14:15], v[24:25] op_sel_hi:[1,0] neg_lo:[0,1] neg_hi:[0,1]
	v_pk_add_f32 v[158:159], v[52:53], v[24:25] op_sel_hi:[1,0] neg_lo:[0,1] neg_hi:[0,1]
	v_pk_add_f32 v[160:161], v[28:29], v[24:25] op_sel_hi:[1,0] neg_lo:[0,1] neg_hi:[0,1]
	v_pk_add_f32 v[156:157], v[32:33], v[24:25] op_sel_hi:[1,0] neg_lo:[0,1] neg_hi:[0,1]
	v_pk_add_f32 v[154:155], v[30:31], v[24:25] op_sel_hi:[1,0] neg_lo:[0,1] neg_hi:[0,1]
	v_pk_add_f32 v[150:151], v[34:35], v[24:25] op_sel_hi:[1,0] neg_lo:[0,1] neg_hi:[0,1]
	v_pk_add_f32 v[152:153], v[16:17], v[24:25] op_sel_hi:[1,0] neg_lo:[0,1] neg_hi:[0,1]
	v_pk_add_f32 v[146:147], v[20:21], v[24:25] op_sel_hi:[1,0] neg_lo:[0,1] neg_hi:[0,1]
	v_pk_add_f32 v[148:149], v[18:19], v[24:25] op_sel_hi:[1,0] neg_lo:[0,1] neg_hi:[0,1]
	v_pk_add_f32 v[142:143], v[22:23], v[24:25] op_sel_hi:[1,0] neg_lo:[0,1] neg_hi:[0,1]
	v_pk_add_f32 v[144:145], v[4:5], v[24:25] op_sel_hi:[1,0] neg_lo:[0,1] neg_hi:[0,1]
	v_pk_add_f32 v[138:139], v[10:11], v[24:25] op_sel_hi:[1,0] neg_lo:[0,1] neg_hi:[0,1]
	v_pk_add_f32 v[140:141], v[6:7], v[24:25] op_sel_hi:[1,0] neg_lo:[0,1] neg_hi:[0,1]
	v_add_f32_e32 v24, v26, v27
	v_add_f32_e32 v24, v36, v24
	v_pk_mul_f32 v[38:39], v[162:163], v[162:163]
	v_add_f32_e32 v24, v37, v24
	v_add_f32_e32 v24, v38, v24
	v_pk_mul_f32 v[14:15], v[164:165], v[164:165]
	v_add_f32_e32 v24, v39, v24
	v_add_f32_e32 v14, v14, v24
	v_pk_mul_f32 v[40:41], v[158:159], v[158:159]
	v_add_f32_e32 v14, v15, v14
	v_add_f32_e32 v14, v40, v14
	v_pk_mul_f32 v[28:29], v[160:161], v[160:161]
	v_add_f32_e32 v14, v41, v14
	v_add_f32_e32 v14, v28, v14
	v_pk_mul_f32 v[32:33], v[156:157], v[156:157]
	v_add_f32_e32 v14, v29, v14
	v_add_f32_e32 v14, v32, v14
	v_pk_mul_f32 v[30:31], v[154:155], v[154:155]
	v_add_f32_e32 v14, v33, v14
	v_add_f32_e32 v14, v30, v14
	v_pk_mul_f32 v[34:35], v[150:151], v[150:151]
	v_add_f32_e32 v14, v31, v14
	v_add_f32_e32 v14, v34, v14
	v_pk_mul_f32 v[16:17], v[152:153], v[152:153]
	v_add_f32_e32 v14, v35, v14
	v_add_f32_e32 v14, v16, v14
	v_pk_mul_f32 v[20:21], v[146:147], v[146:147]
	v_add_f32_e32 v14, v17, v14
	v_add_f32_e32 v14, v20, v14
	v_pk_mul_f32 v[18:19], v[148:149], v[148:149]
	v_add_f32_e32 v14, v21, v14
	v_add_f32_e32 v14, v18, v14
	v_pk_mul_f32 v[22:23], v[142:143], v[142:143]
	v_add_f32_e32 v14, v19, v14
	v_add_f32_e32 v14, v22, v14
	v_pk_mul_f32 v[4:5], v[144:145], v[144:145]
	v_add_f32_e32 v14, v23, v14
	v_add_f32_e32 v4, v4, v14
	v_pk_mul_f32 v[6:7], v[140:141], v[140:141]
	v_add_f32_e32 v4, v5, v4
	v_add_f32_e32 v4, v6, v4
	v_pk_mul_f32 v[10:11], v[138:139], v[138:139]
	v_add_f32_e32 v4, v7, v4
	v_add_f32_e32 v4, v10, v4
	v_add_f32_e32 v4, v11, v4
	ds_bpermute_b32 v5, v176, v4
	global_load_dwordx4 v[96:99], v[8:9], off offset:1024
	global_load_dwordx4 v[92:95], v[12:13], off offset:1024
	global_load_dwordx4 v[84:87], v[42:43], off offset:2048
	global_load_dwordx4 v[72:75], v[42:43], off offset:3072
	global_load_dwordx4 v[88:91], v[8:9], off offset:2048
	global_load_dwordx4 v[76:79], v[8:9], off offset:3072
	global_load_dwordx4 v[80:83], v[12:13], off offset:2048
	global_load_dwordx4 v[68:71], v[12:13], off offset:3072
	global_load_dwordx4 v[44:47], v[122:123], off offset:16
	global_load_dwordx4 v[60:63], v[122:123], off
	global_load_dwordx4 v[52:55], v[124:125], off offset:16
	global_load_dwordx4 v[64:67], v[124:125], off
	global_load_dwordx4 v[36:39], v[122:123], off offset:2064
	global_load_dwordx4 v[48:51], v[122:123], off offset:2048
	global_load_dwordx4 v[40:43], v[124:125], off offset:2064
	global_load_dwordx4 v[56:59], v[124:125], off offset:2048
	s_waitcnt lgkmcnt(0)
	v_add_f32_e32 v4, v4, v5
	ds_bpermute_b32 v5, v177, v4
	s_waitcnt lgkmcnt(0)
	v_add_f32_e32 v4, v4, v5
	ds_bpermute_b32 v5, v178, v4
	s_waitcnt vmcnt(17)
	v_cvt_f32_f16_e32 v184, v108
	v_cvt_f32_f16_sdwa v185, v108 dst_sel:DWORD dst_unused:UNUSED_PAD src0_sel:WORD_1
	v_mov_b32_e32 v108, v113
	s_waitcnt vmcnt(16)
	v_cvt_f32_f16_sdwa v113, v100 dst_sel:DWORD dst_unused:UNUSED_PAD src0_sel:WORD_1
	s_waitcnt lgkmcnt(0)
	v_add_f32_e32 v4, v4, v5
	ds_bpermute_b32 v5, v179, v4
	v_pk_mul_f32 v[184:185], v[108:109], v[184:185] op_sel_hi:[0,1]
	s_waitcnt lgkmcnt(0)
	v_add_f32_e32 v4, v4, v5
	ds_bpermute_b32 v5, v180, v4
	s_waitcnt lgkmcnt(0)
	v_add_f32_e32 v4, v4, v5
	ds_bpermute_b32 v5, v181, v4
	s_waitcnt lgkmcnt(0)
	v_add_f32_e32 v4, v4, v5
	v_fmamk_f32 v4, v4, 0x3a000000, v173
	v_mul_f32_e32 v5, 0x4f800000, v4
	v_cmp_gt_f32_e32 vcc, s48, v4
	s_nop 1
	v_cndmask_b32_e32 v12, v4, v5, vcc
	v_sqrt_f32_e32 v13, v12
	global_load_dwordx4 v[4:7], v[126:127], off offset:16
	global_load_dwordx4 v[24:27], v[126:127], off
	global_load_dwordx4 v[8:11], v[128:129], off offset:16
	global_load_dwordx4 v[32:35], v[128:129], off
	v_add_u32_e32 v14, -1, v13
	v_fma_f32 v15, -v14, v13, v12
	v_cmp_ge_f32_e64 s[0:1], 0, v15
	v_add_u32_e32 v15, 1, v13
	s_nop 0
	v_cndmask_b32_e64 v14, v13, v14, s[0:1]
	v_fma_f32 v13, -v15, v13, v12
	v_cmp_lt_f32_e64 s[0:1], 0, v13
	s_nop 1
	v_cndmask_b32_e64 v13, v14, v15, s[0:1]
	v_mul_f32_e32 v14, 0x37800000, v13
	v_cndmask_b32_e32 v13, v13, v14, vcc
	v_cmp_class_f32_e32 vcc, v12, v174
	s_nop 1
	v_cndmask_b32_e32 v186, v13, v12, vcc
	v_div_scale_f32 v112, s[0:1], v186, v186, 1.0
	v_rcp_f32_e32 v187, v112
	s_lshl_b64 s[0:1], s[4:5], 13
	global_load_dwordx4 v[12:15], v[130:131], off offset:16
	global_load_dwordx4 v[20:23], v[130:131], off
	global_load_dwordx4 v[16:19], v[132:133], off offset:16
	global_load_dwordx4 v[28:31], v[132:133], off
	s_cmp_lg_u32 s12, s4
	v_fma_f32 v182, -v112, v187, 1.0
	v_fmac_f32_e32 v187, v182, v187
	v_div_scale_f32 v182, vcc, 1.0, v186, 1.0
	v_mul_f32_e32 v188, v182, v187
	v_fma_f32 v183, -v112, v188, v182
	v_fmac_f32_e32 v188, v183, v187
	v_fma_f32 v189, -v112, v188, v182
	v_cvt_f32_f16_e32 v182, v0
	v_cvt_f32_f16_sdwa v183, v0 dst_sel:DWORD dst_unused:UNUSED_PAD src0_sel:WORD_1
	v_cvt_f32_f16_e32 v112, v100
	v_cvt_f32_f16_e32 v0, v1
	v_cvt_f32_f16_sdwa v1, v1 dst_sel:DWORD dst_unused:UNUSED_PAD src0_sel:WORD_1
	v_pk_fma_f32 v[182:183], v[182:183], s[10:11], v[184:185] op_sel_hi:[1,0,1]
	v_cvt_f32_f16_e32 v100, v101
	v_pk_fma_f32 v[112:113], v[114:115], v[112:113], v[182:183] op_sel_hi:[0,1,1]
	v_cvt_f32_f16_e32 v182, v109
	v_cvt_f32_f16_sdwa v183, v109 dst_sel:DWORD dst_unused:UNUSED_PAD src0_sel:WORD_1
	v_add_f32_e32 v184, 0, v112
	v_cvt_f32_f16_sdwa v101, v101 dst_sel:DWORD dst_unused:UNUSED_PAD src0_sel:WORD_1
	v_add_f32_e32 v109, v113, v184
	v_pk_mul_f32 v[182:183], v[108:109], v[182:183] op_sel_hi:[0,1]
	v_pk_fma_f32 v[0:1], v[0:1], s[10:11], v[182:183] op_sel_hi:[1,0,1]
	v_cvt_f32_f16_e32 v182, v110
	v_cvt_f32_f16_sdwa v183, v110 dst_sel:DWORD dst_unused:UNUSED_PAD src0_sel:WORD_1
	v_pk_fma_f32 v[0:1], v[114:115], v[100:101], v[0:1] op_sel_hi:[0,1,1]
	v_cvt_f32_f16_e32 v100, v2
	v_cvt_f32_f16_sdwa v101, v2 dst_sel:DWORD dst_unused:UNUSED_PAD src0_sel:WORD_1
	v_cvt_f32_f16_e32 v184, v102
	v_cvt_f32_f16_sdwa v185, v102 dst_sel:DWORD dst_unused:UNUSED_PAD src0_sel:WORD_1
	v_add_f32_e32 v109, v0, v109
	v_pk_mul_f32 v[182:183], v[108:109], v[182:183] op_sel_hi:[0,1]
	v_pk_fma_f32 v[100:101], v[100:101], s[10:11], v[182:183] op_sel_hi:[1,0,1]
	v_add_f32_e32 v2, v1, v109
	v_pk_fma_f32 v[100:101], v[114:115], v[184:185], v[100:101] op_sel_hi:[0,1,1]
	v_cvt_f32_f16_e32 v110, v111
	v_cvt_f32_f16_sdwa v111, v111 dst_sel:DWORD dst_unused:UNUSED_PAD src0_sel:WORD_1
	v_add_f32_e32 v109, v100, v2
	v_cvt_f32_f16_e32 v2, v3
	v_cvt_f32_f16_sdwa v3, v3 dst_sel:DWORD dst_unused:UNUSED_PAD src0_sel:WORD_1
	v_cvt_f32_f16_e32 v102, v103
	v_cvt_f32_f16_sdwa v103, v103 dst_sel:DWORD dst_unused:UNUSED_PAD src0_sel:WORD_1
	v_add_f32_e32 v109, v101, v109
	v_pk_mul_f32 v[110:111], v[108:109], v[110:111] op_sel_hi:[0,1]
	v_pk_fma_f32 v[2:3], v[2:3], s[10:11], v[110:111] op_sel_hi:[1,0,1]
	s_waitcnt vmcnt(23)
	v_cvt_f32_f16_e32 v110, v96
	v_cvt_f32_f16_sdwa v111, v96 dst_sel:DWORD dst_unused:UNUSED_PAD src0_sel:WORD_1
	v_pk_fma_f32 v[2:3], v[114:115], v[102:103], v[2:3] op_sel_hi:[0,1,1]
	v_cvt_f32_f16_e32 v102, v104
	v_cvt_f32_f16_sdwa v103, v104 dst_sel:DWORD dst_unused:UNUSED_PAD src0_sel:WORD_1
	s_waitcnt vmcnt(22)
	v_cvt_f32_f16_e32 v182, v92
	v_cvt_f32_f16_sdwa v183, v92 dst_sel:DWORD dst_unused:UNUSED_PAD src0_sel:WORD_1
	v_add_f32_e32 v109, v2, v109
	v_pk_mul_f32 v[110:111], v[108:109], v[110:111] op_sel_hi:[0,1]
	v_pk_fma_f32 v[102:103], v[102:103], s[10:11], v[110:111] op_sel_hi:[1,0,1]
	v_cvt_f32_f16_e32 v96, v97
	v_cvt_f32_f16_sdwa v97, v97 dst_sel:DWORD dst_unused:UNUSED_PAD src0_sel:WORD_1
	v_add_f32_e32 v92, v3, v109
	v_pk_fma_f32 v[102:103], v[114:115], v[182:183], v[102:103] op_sel_hi:[0,1,1]
	v_cvt_f32_f16_e32 v104, v105
	v_cvt_f32_f16_sdwa v105, v105 dst_sel:DWORD dst_unused:UNUSED_PAD src0_sel:WORD_1
	v_add_f32_e32 v109, v102, v92
	v_cvt_f32_f16_e32 v92, v93
	v_cvt_f32_f16_sdwa v93, v93 dst_sel:DWORD dst_unused:UNUSED_PAD src0_sel:WORD_1
	v_add_f32_e32 v109, v103, v109
	v_pk_mul_f32 v[96:97], v[108:109], v[96:97] op_sel_hi:[0,1]
	v_pk_fma_f32 v[96:97], v[104:105], s[10:11], v[96:97] op_sel_hi:[1,0,1]
	v_cvt_f32_f16_e32 v104, v98
	v_cvt_f32_f16_sdwa v105, v98 dst_sel:DWORD dst_unused:UNUSED_PAD src0_sel:WORD_1
	v_pk_fma_f32 v[92:93], v[114:115], v[92:93], v[96:97] op_sel_hi:[0,1,1]
	v_cvt_f32_f16_e32 v96, v106
	v_cvt_f32_f16_sdwa v97, v106 dst_sel:DWORD dst_unused:UNUSED_PAD src0_sel:WORD_1
	v_cvt_f32_f16_e32 v110, v94
	v_cvt_f32_f16_sdwa v111, v94 dst_sel:DWORD dst_unused:UNUSED_PAD src0_sel:WORD_1
	v_add_f32_e32 v109, v92, v109
	v_pk_mul_f32 v[104:105], v[108:109], v[104:105] op_sel_hi:[0,1]
	v_pk_fma_f32 v[96:97], v[96:97], s[10:11], v[104:105] op_sel_hi:[1,0,1]
	v_cvt_f32_f16_e32 v98, v99
	v_cvt_f32_f16_sdwa v99, v99 dst_sel:DWORD dst_unused:UNUSED_PAD src0_sel:WORD_1
	v_add_f32_e32 v94, v93, v109
	v_pk_fma_f32 v[96:97], v[114:115], v[110:111], v[96:97] op_sel_hi:[0,1,1]
	v_cvt_f32_f16_e32 v104, v107
	v_cvt_f32_f16_sdwa v105, v107 dst_sel:DWORD dst_unused:UNUSED_PAD src0_sel:WORD_1
	v_add_f32_e32 v106, v96, v94
	v_cvt_f32_f16_e32 v94, v95
	v_cvt_f32_f16_sdwa v95, v95 dst_sel:DWORD dst_unused:UNUSED_PAD src0_sel:WORD_1
	v_pk_mul_f32 v[98:99], v[108:109], v[98:99] op_sel_hi:[0,1]
	v_pk_fma_f32 v[98:99], v[104:105], s[10:11], v[98:99] op_sel_hi:[1,0,1]
	s_waitcnt vmcnt(19)
	v_cvt_f32_f16_e32 v104, v88
	v_cvt_f32_f16_sdwa v105, v88 dst_sel:DWORD dst_unused:UNUSED_PAD src0_sel:WORD_1
	v_add_f32_e32 v106, v97, v106
	v_pk_fma_f32 v[94:95], v[114:115], v[94:95], v[98:99] op_sel_hi:[0,1,1]
	v_cvt_f32_f16_e32 v98, v84
	v_cvt_f32_f16_sdwa v99, v84 dst_sel:DWORD dst_unused:UNUSED_PAD src0_sel:WORD_1
	v_add_f32_e32 v109, v94, v106
	s_waitcnt vmcnt(17)
	v_cvt_f32_f16_e32 v106, v80
	v_cvt_f32_f16_sdwa v107, v80 dst_sel:DWORD dst_unused:UNUSED_PAD src0_sel:WORD_1
	v_pk_mul_f32 v[104:105], v[108:109], v[104:105] op_sel_hi:[0,1]
	v_pk_fma_f32 v[98:99], v[98:99], s[10:11], v[104:105] op_sel_hi:[1,0,1]
	v_cvt_f32_f16_e32 v88, v89
	v_cvt_f32_f16_sdwa v89, v89 dst_sel:DWORD dst_unused:UNUSED_PAD src0_sel:WORD_1
	v_add_f32_e32 v80, v95, v109
	v_pk_fma_f32 v[98:99], v[114:115], v[106:107], v[98:99] op_sel_hi:[0,1,1]
	v_cvt_f32_f16_e32 v84, v85
	v_cvt_f32_f16_sdwa v85, v85 dst_sel:DWORD dst_unused:UNUSED_PAD src0_sel:WORD_1
	v_add_f32_e32 v104, v98, v80
	v_cvt_f32_f16_e32 v80, v81
	v_cvt_f32_f16_sdwa v81, v81 dst_sel:DWORD dst_unused:UNUSED_PAD src0_sel:WORD_1
	v_pk_mul_f32 v[88:89], v[108:109], v[88:89] op_sel_hi:[0,1]
	v_pk_fma_f32 v[84:85], v[84:85], s[10:11], v[88:89] op_sel_hi:[1,0,1]
	v_cvt_f32_f16_e32 v88, v90
	v_cvt_f32_f16_sdwa v89, v90 dst_sel:DWORD dst_unused:UNUSED_PAD src0_sel:WORD_1
	v_add_f32_e32 v104, v99, v104
	v_pk_fma_f32 v[80:81], v[114:115], v[80:81], v[84:85] op_sel_hi:[0,1,1]
	v_cvt_f32_f16_e32 v84, v86
	v_cvt_f32_f16_sdwa v85, v86 dst_sel:DWORD dst_unused:UNUSED_PAD src0_sel:WORD_1
	v_add_f32_e32 v106, v80, v104
	v_cvt_f32_f16_e32 v104, v82
	v_cvt_f32_f16_sdwa v105, v82 dst_sel:DWORD dst_unused:UNUSED_PAD src0_sel:WORD_1
	v_pk_mul_f32 v[88:89], v[108:109], v[88:89] op_sel_hi:[0,1]
	v_pk_fma_f32 v[84:85], v[84:85], s[10:11], v[88:89] op_sel_hi:[1,0,1]
	v_cvt_f32_f16_e32 v88, v91
	v_cvt_f32_f16_sdwa v89, v91 dst_sel:DWORD dst_unused:UNUSED_PAD src0_sel:WORD_1
	v_add_f32_e32 v82, v81, v106
	v_pk_fma_f32 v[84:85], v[114:115], v[104:105], v[84:85] op_sel_hi:[0,1,1]
	v_cvt_f32_f16_e32 v86, v87
	v_cvt_f32_f16_sdwa v87, v87 dst_sel:DWORD dst_unused:UNUSED_PAD src0_sel:WORD_1
	v_add_f32_e32 v90, v84, v82
	v_cvt_f32_f16_e32 v82, v83
	v_cvt_f32_f16_sdwa v83, v83 dst_sel:DWORD dst_unused:UNUSED_PAD src0_sel:WORD_1
	v_pk_mul_f32 v[88:89], v[108:109], v[88:89] op_sel_hi:[0,1]
	v_pk_fma_f32 v[86:87], v[86:87], s[10:11], v[88:89] op_sel_hi:[1,0,1]
	v_cvt_f32_f16_e32 v88, v76
	v_cvt_f32_f16_sdwa v89, v76 dst_sel:DWORD dst_unused:UNUSED_PAD src0_sel:WORD_1
	v_add_f32_e32 v90, v85, v90
	v_pk_fma_f32 v[82:83], v[114:115], v[82:83], v[86:87] op_sel_hi:[0,1,1]
	v_cvt_f32_f16_e32 v86, v72
	v_cvt_f32_f16_sdwa v87, v72 dst_sel:DWORD dst_unused:UNUSED_PAD src0_sel:WORD_1
	v_add_f32_e32 v104, v82, v90
	s_waitcnt vmcnt(16)
	v_cvt_f32_f16_e32 v90, v68
	v_cvt_f32_f16_sdwa v91, v68 dst_sel:DWORD dst_unused:UNUSED_PAD src0_sel:WORD_1
	v_pk_mul_f32 v[88:89], v[108:109], v[88:89] op_sel_hi:[0,1]
	v_pk_fma_f32 v[86:87], v[86:87], s[10:11], v[88:89] op_sel_hi:[1,0,1]
	v_cvt_f32_f16_e32 v76, v77
	v_cvt_f32_f16_sdwa v77, v77 dst_sel:DWORD dst_unused:UNUSED_PAD src0_sel:WORD_1
	v_add_f32_e32 v68, v83, v104
	v_pk_fma_f32 v[86:87], v[114:115], v[90:91], v[86:87] op_sel_hi:[0,1,1]
	v_cvt_f32_f16_e32 v72, v73
	v_cvt_f32_f16_sdwa v73, v73 dst_sel:DWORD dst_unused:UNUSED_PAD src0_sel:WORD_1
	v_add_f32_e32 v88, v86, v68
	v_cvt_f32_f16_e32 v68, v69
	v_cvt_f32_f16_sdwa v69, v69 dst_sel:DWORD dst_unused:UNUSED_PAD src0_sel:WORD_1
	v_pk_mul_f32 v[76:77], v[108:109], v[76:77] op_sel_hi:[0,1]
	v_pk_fma_f32 v[72:73], v[72:73], s[10:11], v[76:77] op_sel_hi:[1,0,1]
	v_cvt_f32_f16_e32 v76, v78
	v_cvt_f32_f16_sdwa v77, v78 dst_sel:DWORD dst_unused:UNUSED_PAD src0_sel:WORD_1
	v_add_f32_e32 v88, v87, v88
	v_pk_fma_f32 v[68:69], v[114:115], v[68:69], v[72:73] op_sel_hi:[0,1,1]
	v_cvt_f32_f16_e32 v72, v74
	v_cvt_f32_f16_sdwa v73, v74 dst_sel:DWORD dst_unused:UNUSED_PAD src0_sel:WORD_1
	v_add_f32_e32 v90, v68, v88
	v_cvt_f32_f16_e32 v88, v70
	v_cvt_f32_f16_sdwa v89, v70 dst_sel:DWORD dst_unused:UNUSED_PAD src0_sel:WORD_1
	v_pk_mul_f32 v[76:77], v[108:109], v[76:77] op_sel_hi:[0,1]
	v_pk_fma_f32 v[72:73], v[72:73], s[10:11], v[76:77] op_sel_hi:[1,0,1]
	v_cvt_f32_f16_e32 v76, v79
	v_cvt_f32_f16_sdwa v77, v79 dst_sel:DWORD dst_unused:UNUSED_PAD src0_sel:WORD_1
	v_add_f32_e32 v70, v69, v90
	v_pk_fma_f32 v[72:73], v[114:115], v[88:89], v[72:73] op_sel_hi:[0,1,1]
	v_cvt_f32_f16_e32 v74, v75
	v_cvt_f32_f16_sdwa v75, v75 dst_sel:DWORD dst_unused:UNUSED_PAD src0_sel:WORD_1
	v_add_f32_e32 v78, v72, v70
	v_cvt_f32_f16_e32 v70, v71
	v_cvt_f32_f16_sdwa v71, v71 dst_sel:DWORD dst_unused:UNUSED_PAD src0_sel:WORD_1
	v_pk_mul_f32 v[76:77], v[108:109], v[76:77] op_sel_hi:[0,1]
	v_pk_fma_f32 v[74:75], v[74:75], s[10:11], v[76:77] op_sel_hi:[1,0,1]
	v_add_f32_e32 v78, v73, v78
	v_pk_fma_f32 v[70:71], v[114:115], v[70:71], v[74:75] op_sel_hi:[0,1,1]
	v_add_f32_e32 v74, v70, v78
	v_add_f32_e32 v75, v71, v74
	ds_bpermute_b32 v88, v176, v75
	v_div_fmas_f32 v74, v189, v187, v188
	v_div_fixup_f32 v74, v74, v186, 1.0
	v_pk_mul_f32 v[76:77], v[166:167], v[74:75] op_sel_hi:[1,0]
	v_pk_mul_f32 v[78:79], v[168:169], v[74:75] op_sel_hi:[1,0]
	s_waitcnt lgkmcnt(0)
	v_add_f32_e32 v75, v75, v88
	ds_bpermute_b32 v88, v177, v75
	s_waitcnt vmcnt(12)
	v_pk_fma_f32 v[60:61], v[60:61], v[76:77], v[64:65]
	v_pk_fma_f32 v[62:63], v[62:63], v[78:79], v[66:67]
	v_lshl_add_u64 v[66:67], v[118:119], 0, s[0:1]
	global_store_dwordx4 v[66:67], v[60:63], off nt
	s_waitcnt lgkmcnt(0)
	v_add_f32_e32 v64, v75, v88
	ds_bpermute_b32 v65, v178, v64
	v_pk_mul_f32 v[62:63], v[164:165], v[74:75] op_sel_hi:[1,0]
	v_pk_mul_f32 v[60:61], v[162:163], v[74:75] op_sel_hi:[1,0]
	v_pk_fma_f32 v[46:47], v[46:47], v[62:63], v[54:55]
	v_pk_fma_f32 v[44:45], v[44:45], v[60:61], v[52:53]
	s_waitcnt lgkmcnt(0)
	v_add_f32_e32 v54, v64, v65
	ds_bpermute_b32 v55, v179, v54
	global_store_dwordx4 v[66:67], v[44:47], off offset:16 nt
	s_waitcnt lgkmcnt(0)
	v_add_f32_e32 v52, v54, v55
	ds_bpermute_b32 v53, v180, v52
	v_pk_mul_f32 v[44:45], v[158:159], v[74:75] op_sel_hi:[1,0]
	v_pk_mul_f32 v[46:47], v[160:161], v[74:75] op_sel_hi:[1,0]
	s_waitcnt vmcnt(10)
	v_pk_fma_f32 v[44:45], v[48:49], v[44:45], v[56:57]
	v_pk_fma_f32 v[46:47], v[50:51], v[46:47], v[58:59]
	s_waitcnt lgkmcnt(0)
	v_add_f32_e32 v48, v52, v53
	ds_bpermute_b32 v49, v181, v48
	global_store_dwordx4 v[66:67], v[44:47], off offset:2048 nt
	s_nop 1
	v_pk_mul_f32 v[44:45], v[156:157], v[74:75] op_sel_hi:[1,0]
	v_pk_mul_f32 v[46:47], v[154:155], v[74:75] op_sel_hi:[1,0]
	v_pk_fma_f32 v[36:37], v[36:37], v[44:45], v[40:41]
	v_pk_fma_f32 v[38:39], v[38:39], v[46:47], v[42:43]
	global_store_dwordx4 v[66:67], v[36:39], off offset:2064 nt
	s_waitcnt lgkmcnt(0)
	s_nop 0
	v_add_f32_e32 v36, v48, v49
	v_mul_f32_e32 v64, 0x3a000000, v36
	v_pk_add_f32 v[36:37], v[112:113], v[64:65] op_sel_hi:[1,0] neg_lo:[0,1] neg_hi:[0,1]
	v_pk_add_f32 v[38:39], v[0:1], v[64:65] op_sel_hi:[1,0] neg_lo:[0,1] neg_hi:[0,1]
	v_pk_mul_f32 v[76:77], v[36:37], v[36:37]
	v_pk_mul_f32 v[78:79], v[38:39], v[38:39]
	v_add_f32_e32 v75, v76, v77
	v_pk_add_f32 v[0:1], v[100:101], v[64:65] op_sel_hi:[1,0] neg_lo:[0,1] neg_hi:[0,1]
	v_add_f32_e32 v75, v78, v75
	v_pk_mul_f32 v[88:89], v[0:1], v[0:1]
	v_add_f32_e32 v75, v79, v75
	v_pk_add_f32 v[40:41], v[2:3], v[64:65] op_sel_hi:[1,0] neg_lo:[0,1] neg_hi:[0,1]
	v_add_f32_e32 v75, v88, v75
	v_pk_mul_f32 v[2:3], v[40:41], v[40:41]
	v_add_f32_e32 v75, v89, v75
	v_pk_add_f32 v[42:43], v[102:103], v[64:65] op_sel_hi:[1,0] neg_lo:[0,1] neg_hi:[0,1]
	v_add_f32_e32 v2, v2, v75
	v_pk_mul_f32 v[90:91], v[42:43], v[42:43]
	v_add_f32_e32 v2, v3, v2
	v_pk_add_f32 v[44:45], v[92:93], v[64:65] op_sel_hi:[1,0] neg_lo:[0,1] neg_hi:[0,1]
	v_add_f32_e32 v2, v90, v2
	v_pk_mul_f32 v[92:93], v[44:45], v[44:45]
	v_add_f32_e32 v2, v91, v2
	v_pk_add_f32 v[46:47], v[96:97], v[64:65] op_sel_hi:[1,0] neg_lo:[0,1] neg_hi:[0,1]
	v_add_f32_e32 v2, v92, v2
	v_pk_mul_f32 v[96:97], v[46:47], v[46:47]
	v_add_f32_e32 v2, v93, v2
	v_pk_add_f32 v[48:49], v[94:95], v[64:65] op_sel_hi:[1,0] neg_lo:[0,1] neg_hi:[0,1]
	v_add_f32_e32 v2, v96, v2
	v_pk_mul_f32 v[94:95], v[48:49], v[48:49]
	v_add_f32_e32 v2, v97, v2
	v_pk_add_f32 v[50:51], v[98:99], v[64:65] op_sel_hi:[1,0] neg_lo:[0,1] neg_hi:[0,1]
	v_add_f32_e32 v2, v94, v2
	v_pk_mul_f32 v[98:99], v[50:51], v[50:51]
	v_add_f32_e32 v2, v95, v2
	v_pk_add_f32 v[52:53], v[80:81], v[64:65] op_sel_hi:[1,0] neg_lo:[0,1] neg_hi:[0,1]
	v_add_f32_e32 v2, v98, v2
	v_pk_mul_f32 v[80:81], v[52:53], v[52:53]
	v_add_f32_e32 v2, v99, v2
	v_pk_add_f32 v[54:55], v[84:85], v[64:65] op_sel_hi:[1,0] neg_lo:[0,1] neg_hi:[0,1]
	v_add_f32_e32 v2, v80, v2
	v_pk_mul_f32 v[84:85], v[54:55], v[54:55]
	v_add_f32_e32 v2, v81, v2
	v_pk_add_f32 v[56:57], v[82:83], v[64:65] op_sel_hi:[1,0] neg_lo:[0,1] neg_hi:[0,1]
	v_add_f32_e32 v2, v84, v2
	v_pk_mul_f32 v[82:83], v[56:57], v[56:57]
	v_add_f32_e32 v2, v85, v2
	v_pk_add_f32 v[58:59], v[86:87], v[64:65] op_sel_hi:[1,0] neg_lo:[0,1] neg_hi:[0,1]
	v_add_f32_e32 v2, v82, v2
	v_pk_mul_f32 v[86:87], v[58:59], v[58:59]
	v_add_f32_e32 v2, v83, v2
	v_pk_add_f32 v[60:61], v[68:69], v[64:65] op_sel_hi:[1,0] neg_lo:[0,1] neg_hi:[0,1]
	v_add_f32_e32 v2, v86, v2
	v_pk_mul_f32 v[68:69], v[60:61], v[60:61]
	v_add_f32_e32 v2, v87, v2
	v_pk_add_f32 v[62:63], v[72:73], v[64:65] op_sel_hi:[1,0] neg_lo:[0,1] neg_hi:[0,1]
	v_add_f32_e32 v2, v68, v2
	v_pk_mul_f32 v[72:73], v[62:63], v[62:63]
	v_add_f32_e32 v2, v69, v2
	v_pk_add_f32 v[64:65], v[70:71], v[64:65] op_sel_hi:[1,0] neg_lo:[0,1] neg_hi:[0,1]
	v_add_f32_e32 v2, v72, v2
	v_pk_mul_f32 v[70:71], v[64:65], v[64:65]
	v_add_f32_e32 v2, v73, v2
	v_add_f32_e32 v2, v70, v2
	v_add_f32_e32 v70, v71, v2
	ds_bpermute_b32 v71, v176, v70
	v_pk_mul_f32 v[2:3], v[150:151], v[74:75] op_sel_hi:[1,0]
	v_pk_mul_f32 v[68:69], v[152:153], v[74:75] op_sel_hi:[1,0]
	s_waitcnt vmcnt(8)
	v_pk_fma_f32 v[24:25], v[24:25], v[2:3], v[32:33]
	v_add_co_u32_e32 v32, vcc, s49, v66
	s_waitcnt lgkmcnt(0)
	v_add_f32_e32 v2, v70, v71
	ds_bpermute_b32 v3, v177, v2
	v_pk_fma_f32 v[26:27], v[26:27], v[68:69], v[34:35]
	v_addc_co_u32_e32 v33, vcc, 0, v67, vcc
	global_store_dwordx4 v[32:33], v[24:27], off nt
	s_waitcnt lgkmcnt(0)
	s_nop 0
	v_add_f32_e32 v26, v2, v3
	ds_bpermute_b32 v27, v178, v26
	v_pk_mul_f32 v[2:3], v[146:147], v[74:75] op_sel_hi:[1,0]
	v_pk_mul_f32 v[24:25], v[148:149], v[74:75] op_sel_hi:[1,0]
	v_pk_fma_f32 v[4:5], v[4:5], v[2:3], v[8:9]
	v_pk_fma_f32 v[6:7], v[6:7], v[24:25], v[10:11]
	s_waitcnt lgkmcnt(0)
	v_add_f32_e32 v8, v26, v27
	ds_bpermute_b32 v9, v179, v8
	global_store_dwordx4 v[32:33], v[4:7], off offset:16 nt
	v_pk_mul_f32 v[2:3], v[142:143], v[74:75] op_sel_hi:[1,0]
	s_waitcnt lgkmcnt(0)
	v_add_f32_e32 v8, v8, v9
	ds_bpermute_b32 v9, v180, v8
	v_pk_mul_f32 v[4:5], v[144:145], v[74:75] op_sel_hi:[1,0]
	s_waitcnt vmcnt(6)
	v_pk_fma_f32 v[2:3], v[20:21], v[2:3], v[28:29]
	v_pk_fma_f32 v[4:5], v[22:23], v[4:5], v[30:31]
	global_store_dwordx4 v[32:33], v[2:5], off offset:2048 nt
	v_pk_mul_f32 v[6:7], v[138:139], v[74:75] op_sel_hi:[1,0]
	s_waitcnt lgkmcnt(0)
	v_add_f32_e32 v4, v8, v9
	ds_bpermute_b32 v5, v181, v4
	v_pk_mul_f32 v[2:3], v[140:141], v[74:75] op_sel_hi:[1,0]
	v_pk_fma_f32 v[8:9], v[14:15], v[6:7], v[18:19]
	v_pk_fma_f32 v[6:7], v[12:13], v[2:3], v[16:17]
	global_store_dwordx4 v[32:33], v[6:9], off offset:2064 nt
	s_cbranch_scc0 .LBB0_2322
	global_load_dwordx4 v[8:11], v[132:133], off
	global_load_dwordx4 v[12:15], v[132:133], off offset:16
	global_load_dwordx4 v[16:19], v[130:131], off offset:16
	global_load_dwordx4 v[20:23], v[130:131], off
	global_load_dwordx4 v[24:27], v[128:129], off
	global_load_dwordx4 v[28:31], v[128:129], off offset:16
	global_load_dwordx4 v[32:35], v[126:127], off offset:16
	global_load_dwordx4 v[66:69], v[126:127], off
	global_load_dwordx4 v[70:73], v[124:125], off offset:2048
	global_load_dwordx4 v[74:77], v[124:125], off offset:2064
	global_load_dwordx4 v[78:81], v[122:123], off offset:2064
	global_load_dwordx4 v[82:85], v[122:123], off offset:2048
	global_load_dwordx4 v[86:89], v[124:125], off
	global_load_dwordx4 v[90:93], v[124:125], off offset:16
	global_load_dwordx4 v[94:97], v[122:123], off offset:16
	global_load_dwordx4 v[98:101], v[122:123], off
	s_waitcnt lgkmcnt(0)
	v_add_f32_e32 v2, v4, v5
	v_fmamk_f32 v2, v2, 0x3a000000, v173
	v_mul_f32_e32 v3, 0x4f800000, v2
	v_cmp_gt_f32_e32 vcc, s48, v2
	s_mov_b64 s[2:3], -1
	s_nop 0
	v_cndmask_b32_e32 v2, v2, v3, vcc
	v_sqrt_f32_e32 v3, v2
	s_nop 0
	v_add_u32_e32 v4, -1, v3
	v_add_u32_e32 v5, 1, v3
	v_fma_f32 v6, -v4, v3, v2
	v_fma_f32 v7, -v5, v3, v2
	v_cmp_ge_f32_e64 s[0:1], 0, v6
	s_nop 1
	v_cndmask_b32_e64 v3, v3, v4, s[0:1]
	v_cmp_lt_f32_e64 s[0:1], 0, v7
	s_nop 1
	v_cndmask_b32_e64 v3, v3, v5, s[0:1]
	v_mul_f32_e32 v4, 0x37800000, v3
	v_cndmask_b32_e32 v3, v3, v4, vcc
	v_cmp_class_f32_e32 vcc, v2, v174
	s_nop 1
	v_cndmask_b32_e32 v2, v3, v2, vcc
	v_div_scale_f32 v3, s[0:1], v2, v2, 1.0
	v_rcp_f32_e32 v4, v3
	v_div_scale_f32 v5, vcc, 1.0, v2, 1.0
	v_fma_f32 v6, -v3, v4, 1.0
	v_fmac_f32_e32 v4, v6, v4
	v_mul_f32_e32 v6, v5, v4
	v_fma_f32 v7, -v3, v6, v5
	v_fmac_f32_e32 v6, v7, v4
	v_fma_f32 v3, -v3, v6, v5
	v_div_fmas_f32 v3, v3, v4, v6
	v_div_fixup_f32 v2, v3, v2, 1.0
	v_pk_mul_f32 v[4:5], v[64:65], v[2:3] op_sel_hi:[1,0]
	v_pk_mul_f32 v[6:7], v[60:61], v[2:3] op_sel_hi:[1,0]
	v_pk_mul_f32 v[60:61], v[62:63], v[2:3] op_sel_hi:[1,0]
	v_pk_mul_f32 v[58:59], v[58:59], v[2:3] op_sel_hi:[1,0]
	v_pk_mul_f32 v[56:57], v[56:57], v[2:3] op_sel_hi:[1,0]
	v_pk_mul_f32 v[52:53], v[52:53], v[2:3] op_sel_hi:[1,0]
	v_pk_mul_f32 v[54:55], v[54:55], v[2:3] op_sel_hi:[1,0]
	v_pk_mul_f32 v[50:51], v[50:51], v[2:3] op_sel_hi:[1,0]
	v_pk_mul_f32 v[48:49], v[48:49], v[2:3] op_sel_hi:[1,0]
	v_pk_mul_f32 v[44:45], v[44:45], v[2:3] op_sel_hi:[1,0]
	v_pk_mul_f32 v[46:47], v[46:47], v[2:3] op_sel_hi:[1,0]
	v_pk_mul_f32 v[42:43], v[42:43], v[2:3] op_sel_hi:[1,0]
	v_pk_mul_f32 v[40:41], v[40:41], v[2:3] op_sel_hi:[1,0]
	v_pk_mul_f32 v[38:39], v[38:39], v[2:3] op_sel_hi:[1,0]
	v_pk_mul_f32 v[62:63], v[0:1], v[2:3] op_sel_hi:[1,0]
	v_pk_mul_f32 v[36:37], v[36:37], v[2:3] op_sel_hi:[1,0]
	s_waitcnt vmcnt(13)
	v_pk_fma_f32 v[2:3], v[4:5], v[18:19], v[14:15]
	s_waitcnt vmcnt(12)
	v_pk_fma_f32 v[6:7], v[6:7], v[22:23], v[10:11]
	v_pk_fma_f32 v[0:1], v[60:61], v[16:17], v[12:13]
	v_pk_fma_f32 v[4:5], v[58:59], v[20:21], v[8:9]
	s_waitcnt vmcnt(9)
	v_pk_fma_f32 v[10:11], v[56:57], v[34:35], v[30:31]
	s_waitcnt vmcnt(8)
	v_pk_fma_f32 v[14:15], v[52:53], v[68:69], v[26:27]
	v_pk_fma_f32 v[8:9], v[54:55], v[32:33], v[28:29]
	v_pk_fma_f32 v[12:13], v[50:51], v[66:67], v[24:25]
	s_waitcnt vmcnt(5)
	v_pk_fma_f32 v[18:19], v[48:49], v[80:81], v[76:77]
	s_waitcnt vmcnt(4)
	v_pk_fma_f32 v[22:23], v[44:45], v[84:85], v[72:73]
	v_pk_fma_f32 v[16:17], v[46:47], v[78:79], v[74:75]
	v_pk_fma_f32 v[20:21], v[42:43], v[82:83], v[70:71]
	s_waitcnt vmcnt(1)
	v_pk_fma_f32 v[26:27], v[40:41], v[96:97], v[92:93]
	s_waitcnt vmcnt(0)
	v_pk_fma_f32 v[30:31], v[38:39], v[100:101], v[88:89]
	v_pk_fma_f32 v[24:25], v[62:63], v[94:95], v[90:91]
	v_pk_fma_f32 v[28:29], v[36:37], v[98:99], v[86:87]
.LBB0_2322:
	s_and_b64 vcc, exec, s[2:3]
	s_cbranch_vccz .LBB0_2126
	s_lshl_b64 s[0:1], s[12:13], 13
	v_lshl_add_u64 v[32:33], v[118:119], 0, s[0:1]
	global_store_dwordx4 v[32:33], v[28:31], off nt
	global_store_dwordx4 v[32:33], v[24:27], off offset:16 nt
	global_store_dwordx4 v[32:33], v[20:23], off offset:2048 nt
	global_store_dwordx4 v[32:33], v[16:19], off offset:2064 nt
	s_nop 1
	v_add_co_u32_e32 v16, vcc, 0x1000, v32
	s_nop 1
	v_addc_co_u32_e32 v17, vcc, 0, v33, vcc
	global_store_dwordx4 v[16:17], v[12:15], off nt
	global_store_dwordx4 v[16:17], v[8:11], off offset:16 nt
	s_waitcnt lgkmcnt(0)
	global_store_dwordx4 v[16:17], v[4:7], off offset:2048 nt
	global_store_dwordx4 v[16:17], v[0:3], off offset:2064 nt
	s_branch .LBB0_2126
